# E33: E25 + the first post-barrier LDS wait of the NSA far loops split into counted waits (first QK MFMA starts after 3 of the 6 fragment reads)
# baseline (speedup 1.0000x reference)
.Lr687_skip:
	s_waitcnt lgkmcnt(3)
	v_mfma_f32_16x16x32_bf16 v[90:93], v[70:73], v[78:81], 0
	s_waitcnt lgkmcnt(2)
	v_mfma_f32_16x16x32_bf16 v[70:73], v[70:73], v[82:85], 0
	v_add_u32_e32 v0, s0, v143
	ds_read_b128 v[198:201], v0
	ds_read_b128 v[202:205], v197 offset:1024
	ds_read_b128 v[206:209], v197 offset:5120
	v_mfma_f32_16x16x32_bf16 v[98:101], v[74:77], v[78:81], 0
	v_mfma_f32_16x16x32_bf16 v[74:77], v[74:77], v[82:85], 0
	s_waitcnt lgkmcnt(4)
	v_mfma_f32_16x16x32_bf16 v[210:213], v[86:89], v[78:81], 0
	ds_read_b128 v[214:217], v0 offset:4096
	v_mfma_f32_16x16x32_bf16 v[86:89], v[86:89], v[82:85], 0
	s_waitcnt lgkmcnt(4)
	v_mfma_f32_16x16x32_bf16 v[78:81], v[94:97], v[78:81], 0
	v_mfma_f32_16x16x32_bf16 v[82:85], v[94:97], v[82:85], 0
	ds_read_b128 v[94:97], v0 offset:8192
	s_waitcnt lgkmcnt(3)
	v_mfma_f32_16x16x32_bf16 v[90:93], v[198:201], v[202:205], v[90:93]
	s_waitcnt lgkmcnt(2)
	v_mfma_f32_16x16x32_bf16 v[70:73], v[198:201], v[206:209], v[70:73]
	ds_read_b128 v[198:201], v0 offset:12288
	v_add_u32_e32 v0, s0, v144
	s_waitcnt lgkmcnt(2)
	v_mfma_f32_16x16x32_bf16 v[98:101], v[214:217], v[202:205], v[98:101]
	v_mfma_f32_16x16x32_bf16 v[74:77], v[214:217], v[206:209], v[74:77]
	ds_read_b128 v[214:217], v0
	ds_read_b128 v[218:221], v197 offset:2048
	ds_read_b128 v[222:225], v197 offset:6144
	s_waitcnt lgkmcnt(4)
	v_mfma_f32_16x16x32_bf16 v[210:213], v[94:97], v[202:205], v[210:213]
	v_mfma_f32_16x16x32_bf16 v[86:89], v[94:97], v[206:209], v[86:89]
	ds_read_b128 v[94:97], v0 offset:4096
	s_waitcnt lgkmcnt(4)
	v_mfma_f32_16x16x32_bf16 v[78:81], v[198:201], v[202:205], v[78:81]
	ds_read_b128 v[202:205], v0 offset:8192
	v_mfma_f32_16x16x32_bf16 v[82:85], v[198:201], v[206:209], v[82:85]
	s_waitcnt lgkmcnt(3)
	v_mfma_f32_16x16x32_bf16 v[90:93], v[214:217], v[218:221], v[90:93]
	ds_read_b128 v[198:201], v0 offset:12288
	s_waitcnt lgkmcnt(3)
	v_mfma_f32_16x16x32_bf16 v[70:73], v[214:217], v[222:225], v[70:73]
	v_add_u32_e32 v0, s0, v145
	s_waitcnt lgkmcnt(2)
	v_mfma_f32_16x16x32_bf16 v[206:209], v[94:97], v[218:221], v[98:101]
	v_mfma_f32_16x16x32_bf16 v[74:77], v[94:97], v[222:225], v[74:77]
	ds_read_b128 v[94:97], v0
	ds_read_b128 v[214:217], v197 offset:3072
	ds_read_b128 v[228:231], v197 offset:7168
	s_waitcnt lgkmcnt(4)
	v_mfma_f32_16x16x32_bf16 v[210:213], v[202:205], v[218:221], v[210:213]
	v_mfma_f32_16x16x32_bf16 v[86:89], v[202:205], v[222:225], v[86:89]
	ds_read_b128 v[202:205], v0 offset:4096
	ds_read_b128 v[232:235], v0 offset:8192
	s_waitcnt lgkmcnt(5)
	v_mfma_f32_16x16x32_bf16 v[218:221], v[198:201], v[218:221], v[78:81]
	v_mfma_f32_16x16x32_bf16 v[198:201], v[198:201], v[222:225], v[82:85]
	s_waitcnt lgkmcnt(3)
	v_mfma_f32_16x16x32_bf16 v[82:85], v[94:97], v[214:217], v[90:93]
	ds_read_b128 v[222:225], v0 offset:12288
	s_waitcnt lgkmcnt(3)
	v_mfma_f32_16x16x32_bf16 v[98:101], v[94:97], v[228:231], v[70:73]
	s_waitcnt lgkmcnt(2)
	v_mfma_f32_16x16x32_bf16 v[78:81], v[202:205], v[214:217], v[206:209]
	v_mfma_f32_16x16x32_bf16 v[94:97], v[202:205], v[228:231], v[74:77]
	s_waitcnt lgkmcnt(1)
	v_mfma_f32_16x16x32_bf16 v[74:77], v[232:235], v[214:217], v[210:213]
	v_mfma_f32_16x16x32_bf16 v[90:93], v[232:235], v[228:231], v[86:89]
	s_nop 0
	v_max_f32_e32 v2, v82, v83
	s_waitcnt lgkmcnt(0)
	v_mfma_f32_16x16x32_bf16 v[70:73], v[222:225], v[214:217], v[218:221]
	s_ashr_i32 s22, s1, 5
	v_max_f32_e32 v125, v84, v85
	v_mfma_f32_16x16x32_bf16 v[86:89], v[222:225], v[228:231], v[198:201]
	v_lshl_add_u32 v134, s22, 2, v148
	ds_read_b32 v5, v196 offset:508
	ds_read_b32 v0, v134
	v_max_f32_e32 v137, v80, v81
	v_max3_f32 v137, v78, v79, v137
	v_max3_f32 v2, v2, v125, v137
	v_max_f32_e32 v125, v76, v77
	v_max_f32_e32 v137, v72, v73
	s_lshl_b32 s0, 1, s1
	v_max3_f32 v125, v74, v75, v125
	v_max3_f32 v137, v70, v71, v137
	s_waitcnt lgkmcnt(0)
	v_and_b32_e32 v0, s0, v0
	v_max3_f32 v2, v2, v125, v137
	v_cmp_ne_u32_e32 vcc, 0, v0
	v_mov_b32_e32 v0, v2
	s_nop 1
	v_permlane16_swap_b32_e32 v2, v0
	v_max_f32_e32 v0, v2, v0
	v_mov_b32_e32 v2, v0
	s_nop 1
	v_permlane32_swap_b32_e32 v0, v2
	v_cndmask_b32_e32 v137, v159, v5, vcc
	v_max_f32_e32 v0, v0, v2
	v_fmamk_f32 v0, v0, 0x3fb8aa3b, v137
	v_max_f32_e32 v125, v133, v0
	v_sub_f32_e32 v0, v133, v125
	v_exp_f32_e32 v2, v0
	s_nop 0
	v_cmp_neq_f32_e32 vcc, 1.0, v2
	s_cbranch_vccz .LBB0_695
	v_pk_mul_f32 v[68:69], v[68:69], v[2:3] op_sel_hi:[1,0]
	v_pk_mul_f32 v[66:67], v[66:67], v[2:3] op_sel_hi:[1,0]
	v_pk_mul_f32 v[64:65], v[64:65], v[2:3] op_sel_hi:[1,0]
	v_pk_mul_f32 v[62:63], v[62:63], v[2:3] op_sel_hi:[1,0]
	v_pk_mul_f32 v[60:61], v[60:61], v[2:3] op_sel_hi:[1,0]
	v_pk_mul_f32 v[58:59], v[58:59], v[2:3] op_sel_hi:[1,0]
	v_pk_mul_f32 v[56:57], v[56:57], v[2:3] op_sel_hi:[1,0]
	v_pk_mul_f32 v[54:55], v[54:55], v[2:3] op_sel_hi:[1,0]
	v_pk_mul_f32 v[52:53], v[52:53], v[2:3] op_sel_hi:[1,0]
	v_pk_mul_f32 v[50:51], v[50:51], v[2:3] op_sel_hi:[1,0]
	v_pk_mul_f32 v[48:49], v[48:49], v[2:3] op_sel_hi:[1,0]
	v_pk_mul_f32 v[46:47], v[46:47], v[2:3] op_sel_hi:[1,0]
	v_pk_mul_f32 v[44:45], v[44:45], v[2:3] op_sel_hi:[1,0]
	v_pk_mul_f32 v[42:43], v[42:43], v[2:3] op_sel_hi:[1,0]
	v_pk_mul_f32 v[40:41], v[40:41], v[2:3] op_sel_hi:[1,0]
	v_pk_mul_f32 v[38:39], v[38:39], v[2:3] op_sel_hi:[1,0]

.Lx791_body:
	s_waitcnt lgkmcnt(3)
	v_mfma_f32_16x16x32_bf16 v[90:93], v[70:73], v[78:81], 0
	s_waitcnt lgkmcnt(2)
	v_mfma_f32_16x16x32_bf16 v[70:73], v[70:73], v[82:85], 0
	v_add_u32_e32 v0, s0, v143
	ds_read_b128 v[198:201], v0
	ds_read_b128 v[202:205], v197 offset:1024
	ds_read_b128 v[206:209], v197 offset:5120
	v_mfma_f32_16x16x32_bf16 v[98:101], v[74:77], v[78:81], 0
	v_mfma_f32_16x16x32_bf16 v[74:77], v[74:77], v[82:85], 0
	s_waitcnt lgkmcnt(4)
	v_mfma_f32_16x16x32_bf16 v[210:213], v[86:89], v[78:81], 0
	ds_read_b128 v[214:217], v0 offset:4096
	v_mfma_f32_16x16x32_bf16 v[86:89], v[86:89], v[82:85], 0
	s_waitcnt lgkmcnt(4)
	v_mfma_f32_16x16x32_bf16 v[78:81], v[94:97], v[78:81], 0
	v_mfma_f32_16x16x32_bf16 v[82:85], v[94:97], v[82:85], 0
	ds_read_b128 v[94:97], v0 offset:8192
	s_waitcnt lgkmcnt(3)
	v_mfma_f32_16x16x32_bf16 v[90:93], v[198:201], v[202:205], v[90:93]
	s_waitcnt lgkmcnt(2)
	v_mfma_f32_16x16x32_bf16 v[70:73], v[198:201], v[206:209], v[70:73]
	ds_read_b128 v[198:201], v0 offset:12288
	v_add_u32_e32 v0, s0, v144
	s_waitcnt lgkmcnt(2)
	v_mfma_f32_16x16x32_bf16 v[98:101], v[214:217], v[202:205], v[98:101]
	v_mfma_f32_16x16x32_bf16 v[74:77], v[214:217], v[206:209], v[74:77]
	ds_read_b128 v[214:217], v0
	ds_read_b128 v[218:221], v197 offset:2048
	ds_read_b128 v[222:225], v197 offset:6144
	s_waitcnt lgkmcnt(4)
	v_mfma_f32_16x16x32_bf16 v[210:213], v[94:97], v[202:205], v[210:213]
	v_mfma_f32_16x16x32_bf16 v[86:89], v[94:97], v[206:209], v[86:89]
	ds_read_b128 v[94:97], v0 offset:4096
	s_waitcnt lgkmcnt(4)
	v_mfma_f32_16x16x32_bf16 v[78:81], v[198:201], v[202:205], v[78:81]
	ds_read_b128 v[202:205], v0 offset:8192
	v_mfma_f32_16x16x32_bf16 v[82:85], v[198:201], v[206:209], v[82:85]
	s_waitcnt lgkmcnt(3)
	v_mfma_f32_16x16x32_bf16 v[90:93], v[214:217], v[218:221], v[90:93]
	ds_read_b128 v[198:201], v0 offset:12288
	s_waitcnt lgkmcnt(3)
	v_mfma_f32_16x16x32_bf16 v[70:73], v[214:217], v[222:225], v[70:73]
	v_add_u32_e32 v0, s0, v145
	s_waitcnt lgkmcnt(2)
	v_mfma_f32_16x16x32_bf16 v[206:209], v[94:97], v[218:221], v[98:101]
	v_mfma_f32_16x16x32_bf16 v[74:77], v[94:97], v[222:225], v[74:77]
	ds_read_b128 v[94:97], v0
	ds_read_b128 v[214:217], v197 offset:3072
	ds_read_b128 v[228:231], v197 offset:7168
	s_waitcnt lgkmcnt(4)
	v_mfma_f32_16x16x32_bf16 v[210:213], v[202:205], v[218:221], v[210:213]
	v_mfma_f32_16x16x32_bf16 v[86:89], v[202:205], v[222:225], v[86:89]
	ds_read_b128 v[202:205], v0 offset:4096
	ds_read_b128 v[232:235], v0 offset:8192
	s_waitcnt lgkmcnt(5)
	v_mfma_f32_16x16x32_bf16 v[218:221], v[198:201], v[218:221], v[78:81]
	v_mfma_f32_16x16x32_bf16 v[198:201], v[198:201], v[222:225], v[82:85]
	s_waitcnt lgkmcnt(3)
	v_mfma_f32_16x16x32_bf16 v[82:85], v[94:97], v[214:217], v[90:93]
	ds_read_b128 v[222:225], v0 offset:12288
	s_waitcnt lgkmcnt(3)
	v_mfma_f32_16x16x32_bf16 v[98:101], v[94:97], v[228:231], v[70:73]
	s_waitcnt lgkmcnt(2)
	v_mfma_f32_16x16x32_bf16 v[78:81], v[202:205], v[214:217], v[206:209]
	v_mfma_f32_16x16x32_bf16 v[94:97], v[202:205], v[228:231], v[74:77]
	s_waitcnt lgkmcnt(1)
	v_mfma_f32_16x16x32_bf16 v[74:77], v[232:235], v[214:217], v[210:213]
	v_mfma_f32_16x16x32_bf16 v[90:93], v[232:235], v[228:231], v[86:89]
	s_nop 0
	v_max_f32_e32 v0, v82, v83
	s_waitcnt lgkmcnt(0)
	v_mfma_f32_16x16x32_bf16 v[70:73], v[222:225], v[214:217], v[218:221]
	v_max_f32_e32 v2, v84, v85
	s_nop 0
	v_max_f32_e32 v5, v80, v81
	v_max3_f32 v5, v78, v79, v5
	v_max3_f32 v0, v0, v2, v5
	v_max_f32_e32 v2, v76, v77
	s_nop 1
	v_max_f32_e32 v5, v72, v73
	v_max3_f32 v2, v74, v75, v2
	v_max3_f32 v5, v70, v71, v5
	v_max3_f32 v0, v0, v2, v5
	v_mov_b32_e32 v2, v0
	s_nop 1
	v_permlane16_swap_b32_e32 v0, v2
	ds_read_b32 v125, v196 offset:508
	v_max_f32_e32 v0, v0, v2
	v_mov_b32_e32 v2, v0
	s_nop 1
	v_permlane32_swap_b32_e32 v0, v2
	v_max_f32_e32 v0, v0, v2
	s_waitcnt lgkmcnt(0)
	v_fmamk_f32 v0, v0, 0x3fb8aa3b, v125
	v_max_f32_e32 v133, v137, v0
	v_sub_f32_e32 v0, v137, v133
	v_exp_f32_e32 v2, v0
	v_mfma_f32_16x16x32_bf16 v[86:89], v[222:225], v[228:231], v[198:201]
	v_cmp_neq_f32_e32 vcc, 1.0, v2
	s_cbranch_vccz .LBB0_803
	v_pk_mul_f32 v[68:69], v[68:69], v[2:3] op_sel_hi:[1,0]
	v_pk_mul_f32 v[66:67], v[66:67], v[2:3] op_sel_hi:[1,0]
	v_pk_mul_f32 v[64:65], v[64:65], v[2:3] op_sel_hi:[1,0]
	v_pk_mul_f32 v[62:63], v[62:63], v[2:3] op_sel_hi:[1,0]
	v_pk_mul_f32 v[60:61], v[60:61], v[2:3] op_sel_hi:[1,0]
	v_pk_mul_f32 v[58:59], v[58:59], v[2:3] op_sel_hi:[1,0]
	v_pk_mul_f32 v[56:57], v[56:57], v[2:3] op_sel_hi:[1,0]
	v_pk_mul_f32 v[54:55], v[54:55], v[2:3] op_sel_hi:[1,0]
	v_pk_mul_f32 v[52:53], v[52:53], v[2:3] op_sel_hi:[1,0]
	v_pk_mul_f32 v[50:51], v[50:51], v[2:3] op_sel_hi:[1,0]
	v_pk_mul_f32 v[48:49], v[48:49], v[2:3] op_sel_hi:[1,0]
	v_pk_mul_f32 v[46:47], v[46:47], v[2:3] op_sel_hi:[1,0]
	v_pk_mul_f32 v[44:45], v[44:45], v[2:3] op_sel_hi:[1,0]
	v_pk_mul_f32 v[42:43], v[42:43], v[2:3] op_sel_hi:[1,0]
	v_pk_mul_f32 v[40:41], v[40:41], v[2:3] op_sel_hi:[1,0]
	v_pk_mul_f32 v[38:39], v[38:39], v[2:3] op_sel_hi:[1,0]

.LBB0_808:
	s_sub_i32 s0, s33, s42
	s_sub_i32 s47, s0, s43
	s_add_i32 s23, s37, -1
	s_sub_i32 s81, 0, s42
	s_add_i32 s82, s23, 1
	s_cmp_lt_i32 s82, s42
	s_mov_b64 s[0:1], -1
	s_cbranch_scc1 .LBB0_815
	s_branch .LBB0_810
	s_nop 0
	s_nop 0
	s_nop 0
	s_nop 0
	s_nop 0
	s_nop 0
	s_nop 0
	s_nop 0
	s_nop 0
	s_nop 0
	s_nop 0
	s_nop 0
	s_nop 0
	s_nop 0
	s_nop 0
	s_nop 0
	s_nop 0
	s_nop 0
	s_nop 0
	s_nop 0
	s_nop 0
	s_nop 0
	s_nop 0
	s_nop 0
	s_nop 0
	s_nop 0
	s_nop 0
	s_nop 0
	s_nop 0
	s_nop 0
